# gate/up GEMM (fused-gather path): accumulators zeroed by 32 two-pass 4x4x1 f32 MFMAs per unit instead of 128 v_mov
# speedup vs baseline: 1.0131x; 1.0042x over previous
.LBB0_1105:
	s_ashr_i32 s19, s18, 31
	s_lshl_b64 s[20:21], s[18:19], 18
	s_add_u32 s20, s15, s20
	s_addc_u32 s21, s17, s21
	s_and_b64 s[30:31], s[28:29], exec
	s_cselect_b32 s19, s21, s1
	s_cselect_b32 s57, s20, s0
	s_lshl_b32 s30, s41, 10
	s_add_i32 s30, s30, 0
	s_add_i32 s30, s30, 0x20010
	v_mov_b32_e32 v167, v161
	v_mov_b32_e32 v169, v161
	s_add_u32 s58, s0, 0x100
	v_mov_b32_e32 v32, 0
	v_lshl_add_u32 v199, v184, 2, s30
	v_lshl_add_u32 v200, v188, 2, s30
	v_lshl_add_u64 v[172:173], s[10:11], 0, v[168:169]
	v_lshl_add_u64 v[174:175], s[10:11], 0, v[166:167]
	s_addc_u32 s59, s1, 0
	s_mov_b32 s60, -2
	s_mov_b64 s[30:31], 0
	v_mov_b32_e32 v197, v168
	v_mov_b32_e32 v169, v166
	v_mov_b32_e32 v196, v170
	v_mov_b32_e32 v167, v198
	s_nop 1
	v_mfma_f32_4x4x1_16b_f32 v[36:39], v32, v32, 0
	v_mfma_f32_4x4x1_16b_f32 v[40:43], v32, v32, 0
	v_mfma_f32_4x4x1_16b_f32 v[44:47], v32, v32, 0
	v_mfma_f32_4x4x1_16b_f32 v[48:51], v32, v32, 0
	v_mfma_f32_4x4x1_16b_f32 v[52:55], v32, v32, 0
	v_mfma_f32_4x4x1_16b_f32 v[56:59], v32, v32, 0
	v_mfma_f32_4x4x1_16b_f32 v[60:63], v32, v32, 0
	v_mfma_f32_4x4x1_16b_f32 v[64:67], v32, v32, 0
	v_mfma_f32_4x4x1_16b_f32 v[68:71], v32, v32, 0
	v_mfma_f32_4x4x1_16b_f32 v[72:75], v32, v32, 0
	v_mfma_f32_4x4x1_16b_f32 v[76:79], v32, v32, 0
	v_mfma_f32_4x4x1_16b_f32 v[80:83], v32, v32, 0
	v_mfma_f32_4x4x1_16b_f32 v[84:87], v32, v32, 0
	v_mfma_f32_4x4x1_16b_f32 v[88:91], v32, v32, 0
	v_mfma_f32_4x4x1_16b_f32 v[92:95], v32, v32, 0
	v_mfma_f32_4x4x1_16b_f32 v[96:99], v32, v32, 0
	v_mfma_f32_4x4x1_16b_f32 v[100:103], v32, v32, 0
	v_mfma_f32_4x4x1_16b_f32 v[104:107], v32, v32, 0
	v_mfma_f32_4x4x1_16b_f32 v[108:111], v32, v32, 0
	v_mfma_f32_4x4x1_16b_f32 v[112:115], v32, v32, 0
	v_mfma_f32_4x4x1_16b_f32 v[116:119], v32, v32, 0
	v_mfma_f32_4x4x1_16b_f32 v[120:123], v32, v32, 0
	v_mfma_f32_4x4x1_16b_f32 v[124:127], v32, v32, 0
	v_mfma_f32_4x4x1_16b_f32 v[128:131], v32, v32, 0
	v_mfma_f32_4x4x1_16b_f32 v[132:135], v32, v32, 0
	v_mfma_f32_4x4x1_16b_f32 v[136:139], v32, v32, 0
	v_mfma_f32_4x4x1_16b_f32 v[140:143], v32, v32, 0
	v_mfma_f32_4x4x1_16b_f32 v[144:147], v32, v32, 0
	v_mfma_f32_4x4x1_16b_f32 v[148:151], v32, v32, 0
	v_mfma_f32_4x4x1_16b_f32 v[152:155], v32, v32, 0
	v_mfma_f32_4x4x1_16b_f32 v[156:159], v32, v32, 0
	v_mfma_f32_4x4x1_16b_f32 v[32:35], v32, v32, 0
	s_branch .LBB0_1107
